# P9/P10: experts of all of a workgroup's units found once before the unit loop (lane i of a VGPR = expert of unit i, same compares), unit header takes it with v_readlane; NB from an SGPR
# speedup vs baseline: 1.0154x; 1.0015x over previous
.LBB0_1346:
	s_add_u32 s14, s6, 0x32000000
	s_addc_u32 s15, s7, 0
	s_lshr_b32 s16, s94, 28
	v_readlane_b32 s17, v255, 19
	s_add_i32 s16, s17, s16
	s_ashr_i32 s64, s16, 4
	s_and_b32 s16, s54, 12
	s_lshl_b32 s5, s5, 5
	s_or_b32 s65, s16, s33
	s_mov_b64 s[16:17], 0x80
	s_and_b32 s5, s5, 0x60
	v_lshl_add_u64 v[4:5], v[4:5], 0, s[16:17]
	s_add_i32 m0, s59, 0x18000
	s_lshl_b32 s19, s4, 13
	s_lshl_b32 s22, s5, 7
	s_waitcnt vmcnt(2)
	s_barrier
	global_load_lds_dwordx4 v[4:5], off
	s_add_i32 m0, s59, 0x1a000
	s_add_u32 s20, s6, 0x2e000080
	v_lshl_add_u64 v[2:3], v[2:3], 0, s[16:17]
	s_addc_u32 s21, s7, 0
	s_add_i32 s66, s59, 0x8000
	global_load_lds_dwordx4 v[2:3], off
	v_lshl_add_u64 v[2:3], s[20:21], 0, v[162:163]
	s_mov_b32 m0, s66
	s_add_i32 s67, s59, 0xa000
	global_load_lds_dwordx4 v[2:3], off
	v_lshl_add_u64 v[2:3], s[20:21], 0, v[170:171]
	s_add_u32 s20, s38, 0x40080
	s_mov_b32 m0, s67
	s_addc_u32 s21, s39, 0
	global_load_lds_dwordx4 v[2:3], off
	v_lshl_add_u64 v[2:3], s[20:21], 0, v[164:165]
	s_add_i32 m0, s59, 0x1c000
	v_readfirstlane_b32 s26, v0
	global_load_lds_dwordx4 v[2:3], off
	v_lshl_add_u64 v[2:3], s[20:21], 0, v[166:167]
	s_add_i32 m0, s59, 0x1e000
	s_cmpk_lt_u32 s18, 0x100
	global_load_lds_dwordx4 v[2:3], off
	v_lshrrev_b32_e32 v3, 1, v6
	v_and_b32_e32 v3, 24, v3
	v_and_b32_e32 v2, 15, v6
	v_lshlrev_b32_e32 v4, 1, v3
	v_lshl_or_b32 v171, s4, 6, v2
	v_lshl_or_b32 v2, v2, 6, v4
	v_lshlrev_b32_e32 v4, 2, v6
	v_and_b32_e32 v4, 32, v4
	v_bitop3_b32 v5, v2, s19, v4 bitop3:0xde
	s_waitcnt vmcnt(6)
	s_cselect_b64 s[18:19], -1, 0
	s_add_u32 s20, s6, 0x2e000100
	s_addc_u32 s21, s7, 0
	s_add_i32 s4, 0, 0x210c0
	v_bitop3_b32 v185, v2, s22, v4 bitop3:0xde
	v_or_b32_e32 v186, s5, v3
	v_readfirstlane_b32 s28, v0
	v_mov_b32_e32 v195, s23
	v_mov_b32_e32 v187, s4
	s_add_i32 s68, 0, 0x21044
	s_add_i32 s69, 0, 0x2104c
	s_add_i32 s70, 0, 0x21054
	s_add_i32 s71, 0, 0x2105c
	s_add_i32 s72, 0, 0x21064
	s_add_i32 s73, 0, 0x2106c
	s_add_i32 s75, 0, 0x21074
	s_add_i32 s76, 0, 0x2107c
	s_add_i32 s77, 0, 0x21084
	s_add_i32 s78, 0, 0x2108c
	s_add_i32 s79, 0, 0x21094
	s_add_i32 s80, 0, 0x2109c
	s_add_i32 s81, 0, 0x210a4
	s_add_i32 s82, 0, 0x210ac
	s_add_i32 s83, 0, 0x210b4
	s_add_i32 s84, 0, 0x210bc
	s_add_i32 s85, 0, 0x10000
	s_add_i32 s86, 0, 0x14000
	v_add_u32_e32 v188, 0, v5
	s_mov_b32 s22, 0x3d000000
	s_mov_b32 s87, 0xc0e00000
	s_mov_b32 s24, 0xc01d265f
	v_mov_b32_e32 v189, 0x40e00000
	v_mov_b32_e32 v196, v162
	v_mbcnt_lo_u32_b32 v250, -1, 0
	v_mbcnt_hi_u32_b32 v250, -1, v250
	v_mul_u32_u24_e32 v250, s64, v250
	v_add_u32_e32 v250, s23, v250
	v_mov_b32_e32 v251, 0x21040
	ds_read_b32 v34, v251 offset:4
	ds_read_b32 v35, v251 offset:8
	ds_read_b32 v36, v251 offset:12
	ds_read_b32 v37, v251 offset:16
	ds_read_b32 v38, v251 offset:20
	ds_read_b32 v39, v251 offset:24
	ds_read_b32 v40, v251 offset:28
	ds_read_b32 v41, v251 offset:32
	ds_read_b32 v42, v251 offset:36
	ds_read_b32 v43, v251 offset:40
	ds_read_b32 v44, v251 offset:44
	ds_read_b32 v45, v251 offset:48
	ds_read_b32 v46, v251 offset:52
	ds_read_b32 v47, v251 offset:56
	ds_read_b32 v48, v251 offset:60
	ds_read_b32 v49, v251 offset:64
	ds_read_b32 v50, v251 offset:68
	ds_read_b32 v51, v251 offset:72
	ds_read_b32 v52, v251 offset:76
	ds_read_b32 v53, v251 offset:80
	ds_read_b32 v54, v251 offset:84
	ds_read_b32 v55, v251 offset:88
	ds_read_b32 v56, v251 offset:92
	ds_read_b32 v57, v251 offset:96
	ds_read_b32 v58, v251 offset:100
	ds_read_b32 v59, v251 offset:104
	ds_read_b32 v60, v251 offset:108
	ds_read_b32 v61, v251 offset:112
	ds_read_b32 v62, v251 offset:116
	ds_read_b32 v63, v251 offset:120
	ds_read_b32 v64, v251 offset:124
	ds_read_b32 v65, v251 offset:128
	v_mov_b32_e32 v254, 0
	s_waitcnt lgkmcnt(0)
	v_cmp_ge_i32_e32 vcc, v250, v34
	s_nop 1
	v_addc_co_u32_e32 v254, vcc, 0, v254, vcc
	v_cmp_ge_i32_e32 vcc, v250, v35
	s_nop 1
	v_addc_co_u32_e32 v254, vcc, 0, v254, vcc
	v_cmp_ge_i32_e32 vcc, v250, v36
	s_nop 1
	v_addc_co_u32_e32 v254, vcc, 0, v254, vcc
	v_cmp_ge_i32_e32 vcc, v250, v37
	s_nop 1
	v_addc_co_u32_e32 v254, vcc, 0, v254, vcc
	v_cmp_ge_i32_e32 vcc, v250, v38
	s_nop 1
	v_addc_co_u32_e32 v254, vcc, 0, v254, vcc
	v_cmp_ge_i32_e32 vcc, v250, v39
	s_nop 1
	v_addc_co_u32_e32 v254, vcc, 0, v254, vcc
	v_cmp_ge_i32_e32 vcc, v250, v40
	s_nop 1
	v_addc_co_u32_e32 v254, vcc, 0, v254, vcc
	v_cmp_ge_i32_e32 vcc, v250, v41
	s_nop 1
	v_addc_co_u32_e32 v254, vcc, 0, v254, vcc
	v_cmp_ge_i32_e32 vcc, v250, v42
	s_nop 1
	v_addc_co_u32_e32 v254, vcc, 0, v254, vcc
	v_cmp_ge_i32_e32 vcc, v250, v43
	s_nop 1
	v_addc_co_u32_e32 v254, vcc, 0, v254, vcc
	v_cmp_ge_i32_e32 vcc, v250, v44
	s_nop 1
	v_addc_co_u32_e32 v254, vcc, 0, v254, vcc
	v_cmp_ge_i32_e32 vcc, v250, v45
	s_nop 1
	v_addc_co_u32_e32 v254, vcc, 0, v254, vcc
	v_cmp_ge_i32_e32 vcc, v250, v46
	s_nop 1
	v_addc_co_u32_e32 v254, vcc, 0, v254, vcc
	v_cmp_ge_i32_e32 vcc, v250, v47
	s_nop 1
	v_addc_co_u32_e32 v254, vcc, 0, v254, vcc
	v_cmp_ge_i32_e32 vcc, v250, v48
	s_nop 1
	v_addc_co_u32_e32 v254, vcc, 0, v254, vcc
	v_cmp_ge_i32_e32 vcc, v250, v49
	s_nop 1
	v_addc_co_u32_e32 v254, vcc, 0, v254, vcc
	v_cmp_ge_i32_e32 vcc, v250, v50
	s_nop 1
	v_addc_co_u32_e32 v254, vcc, 0, v254, vcc
	v_cmp_ge_i32_e32 vcc, v250, v51
	s_nop 1
	v_addc_co_u32_e32 v254, vcc, 0, v254, vcc
	v_cmp_ge_i32_e32 vcc, v250, v52
	s_nop 1
	v_addc_co_u32_e32 v254, vcc, 0, v254, vcc
	v_cmp_ge_i32_e32 vcc, v250, v53
	s_nop 1
	v_addc_co_u32_e32 v254, vcc, 0, v254, vcc
	v_cmp_ge_i32_e32 vcc, v250, v54
	s_nop 1
	v_addc_co_u32_e32 v254, vcc, 0, v254, vcc
	v_cmp_ge_i32_e32 vcc, v250, v55
	s_nop 1
	v_addc_co_u32_e32 v254, vcc, 0, v254, vcc
	v_cmp_ge_i32_e32 vcc, v250, v56
	s_nop 1
	v_addc_co_u32_e32 v254, vcc, 0, v254, vcc
	v_cmp_ge_i32_e32 vcc, v250, v57
	s_nop 1
	v_addc_co_u32_e32 v254, vcc, 0, v254, vcc
	v_cmp_ge_i32_e32 vcc, v250, v58
	s_nop 1
	v_addc_co_u32_e32 v254, vcc, 0, v254, vcc
	v_cmp_ge_i32_e32 vcc, v250, v59
	s_nop 1
	v_addc_co_u32_e32 v254, vcc, 0, v254, vcc
	v_cmp_ge_i32_e32 vcc, v250, v60
	s_nop 1
	v_addc_co_u32_e32 v254, vcc, 0, v254, vcc
	v_cmp_ge_i32_e32 vcc, v250, v61
	s_nop 1
	v_addc_co_u32_e32 v254, vcc, 0, v254, vcc
	v_cmp_ge_i32_e32 vcc, v250, v62
	s_nop 1
	v_addc_co_u32_e32 v254, vcc, 0, v254, vcc
	v_cmp_ge_i32_e32 vcc, v250, v63
	s_nop 1
	v_addc_co_u32_e32 v254, vcc, 0, v254, vcc
	v_cmp_ge_i32_e32 vcc, v250, v64
	s_nop 1
	v_addc_co_u32_e32 v254, vcc, 0, v254, vcc
	v_readfirstlane_b32 s100, v65
	s_barrier
	s_branch .LBB0_1349

.LBB0_1349:
	v_mov_b32_e32 v2, s100
	s_add_i32 s63, s63, 1
	s_mul_i32 s4, s63, s64
	s_add_i32 s27, s23, s4
	s_mov_b64 s[40:41], s[20:21]
	s_waitcnt lgkmcnt(0)
	v_cmp_ge_i32_e64 s[6:7], s27, v2
	v_cmp_lt_i32_e64 s[4:5], s27, v2
	s_and_b64 vcc, exec, s[6:7]
	s_cbranch_vccnz .LBB0_1366
	v_mov_b32_e32 v194, s27
	s_mov_b64 s[40:41], s[2:3]
	s_mov_b32 s28, s65
	v_readlane_b32 s26, v254, s63
	s_mov_b64 s[42:43], -1
	s_and_b64 vcc, exec, s[6:7]
	s_cbranch_vccnz .LBB0_1367

.LBB0_1432:
	s_add_u32 s18, s6, 0x44000000
	s_addc_u32 s19, s7, 0
	s_lshl_b32 s6, s20, 5
	s_and_b32 s9, s6, 0x60
	s_lshr_b32 s6, s94, 29
	v_readlane_b32 s7, v255, 19
	s_mov_b64 s[20:21], 0x80
	s_add_i32 s6, s7, s6
	v_lshl_add_u64 v[8:9], v[8:9], 0, s[20:21]
	s_add_i32 m0, s1, 0x18000
	s_lshl_b32 s8, s23, 13
	s_lshl_b32 s11, s9, 7
	s_ashr_i32 s59, s6, 3
	s_waitcnt vmcnt(2)
	s_barrier
	global_load_lds_dwordx4 v[8:9], off
	v_lshl_add_u64 v[4:5], v[4:5], 0, s[20:21]
	s_add_i32 m0, s1, 0x1a000
	s_add_i32 s60, s1, 0x8000
	s_add_i32 s61, s1, 0xa000
	global_load_lds_dwordx4 v[4:5], off
	v_lshl_add_u64 v[2:3], v[2:3], 0, s[20:21]
	s_mov_b32 m0, s60
	s_add_u32 s6, s44, 0x40080
	global_load_lds_dwordx4 v[2:3], off
	v_lshl_add_u64 v[2:3], v[6:7], 0, s[20:21]
	s_mov_b32 m0, s61
	s_addc_u32 s7, s45, 0
	global_load_lds_dwordx4 v[2:3], off
	v_lshl_add_u64 v[2:3], s[6:7], 0, v[164:165]
	s_add_i32 m0, s1, 0x1c000
	v_mov_b32_e32 v171, v165
	global_load_lds_dwordx4 v[2:3], off
	v_lshl_add_u64 v[2:3], s[6:7], 0, v[162:163]
	s_add_i32 m0, s1, 0x1e000
	s_cmpk_lt_u32 s22, 0x100
	global_load_lds_dwordx4 v[2:3], off
	v_lshrrev_b32_e32 v3, 1, v10
	v_and_b32_e32 v3, 24, v3
	v_and_b32_e32 v2, 15, v10
	v_lshlrev_b32_e32 v4, 1, v3
	v_lshl_or_b32 v1, s23, 6, v2
	v_lshl_or_b32 v2, v2, 6, v4
	v_lshlrev_b32_e32 v4, 2, v10
	v_and_b32_e32 v4, 32, v4
	s_waitcnt vmcnt(6)
	v_bitop3_b32 v5, v2, s8, v4 bitop3:0xde
	v_bitop3_b32 v182, v2, s11, v4 bitop3:0xde
	s_cselect_b64 s[22:23], -1, 0
	s_add_i32 s6, 0, 0x210c0
	s_add_i32 s80, 0, 0x10000
	s_add_i32 s81, 0, 0x14000
	v_mov_b32_e32 v173, v165
	s_mov_b32 s62, 0
	v_or_b32_e32 v183, s9, v3
	v_mov_b32_e32 v184, s6
	s_add_i32 s63, 0, 0x21044
	s_add_i32 s64, 0, 0x2104c
	s_add_i32 s65, 0, 0x21054
	s_add_i32 s66, 0, 0x2105c
	s_add_i32 s67, 0, 0x21064
	s_add_i32 s68, 0, 0x2106c
	s_add_i32 s69, 0, 0x21074
	s_add_i32 s70, 0, 0x2107c
	s_add_i32 s71, 0, 0x21084
	s_add_i32 s72, 0, 0x2108c
	s_add_i32 s73, 0, 0x21094
	s_add_i32 s75, 0, 0x2109c
	s_add_i32 s76, 0, 0x210a4
	s_add_i32 s77, 0, 0x210ac
	s_add_i32 s78, 0, 0x210b4
	s_add_i32 s79, 0, 0x210bc
	v_add_u32_e32 v185, s80, v182
	v_add_u32_e32 v186, s81, v182
	v_add_u32_e32 v187, 0, v5
	s_mov_b64 s[24:25], 0x48000
	s_mov_b64 s[26:27], 0x50000
	s_mov_b64 s[28:29], 0x58000
	s_mov_b32 s30, 0x3d000000
	s_mov_b32 s82, 0x48000
	s_mov_b32 s83, 0x50000
	s_mov_b32 s84, 0x58000
	s_mov_b32 s85, s0
	v_mbcnt_lo_u32_b32 v250, -1, 0
	v_mbcnt_hi_u32_b32 v250, -1, v250
	v_mul_u32_u24_e32 v250, s59, v250
	v_add_u32_e32 v250, s98, v250
	v_sub_u32_e32 v250, s99, v250
	v_add_u32_e32 v250, -1, v250
	v_mov_b32_e32 v251, 0x21040
	ds_read_b32 v34, v251 offset:4
	ds_read_b32 v35, v251 offset:8
	ds_read_b32 v36, v251 offset:12
	ds_read_b32 v37, v251 offset:16
	ds_read_b32 v38, v251 offset:20
	ds_read_b32 v39, v251 offset:24
	ds_read_b32 v40, v251 offset:28
	ds_read_b32 v41, v251 offset:32
	ds_read_b32 v42, v251 offset:36
	ds_read_b32 v43, v251 offset:40
	ds_read_b32 v44, v251 offset:44
	ds_read_b32 v45, v251 offset:48
	ds_read_b32 v46, v251 offset:52
	ds_read_b32 v47, v251 offset:56
	ds_read_b32 v48, v251 offset:60
	ds_read_b32 v49, v251 offset:64
	ds_read_b32 v50, v251 offset:68
	ds_read_b32 v51, v251 offset:72
	ds_read_b32 v52, v251 offset:76
	ds_read_b32 v53, v251 offset:80
	ds_read_b32 v54, v251 offset:84
	ds_read_b32 v55, v251 offset:88
	ds_read_b32 v56, v251 offset:92
	ds_read_b32 v57, v251 offset:96
	ds_read_b32 v58, v251 offset:100
	ds_read_b32 v59, v251 offset:104
	ds_read_b32 v60, v251 offset:108
	ds_read_b32 v61, v251 offset:112
	ds_read_b32 v62, v251 offset:116
	ds_read_b32 v63, v251 offset:120
	ds_read_b32 v64, v251 offset:124
	ds_read_b32 v65, v251 offset:128
	v_mov_b32_e32 v254, 0
	s_waitcnt lgkmcnt(0)
	v_cmp_ge_i32_e32 vcc, v250, v34
	s_nop 1
	v_addc_co_u32_e32 v254, vcc, 0, v254, vcc
	v_cmp_ge_i32_e32 vcc, v250, v35
	s_nop 1
	v_addc_co_u32_e32 v254, vcc, 0, v254, vcc
	v_cmp_ge_i32_e32 vcc, v250, v36
	s_nop 1
	v_addc_co_u32_e32 v254, vcc, 0, v254, vcc
	v_cmp_ge_i32_e32 vcc, v250, v37
	s_nop 1
	v_addc_co_u32_e32 v254, vcc, 0, v254, vcc
	v_cmp_ge_i32_e32 vcc, v250, v38
	s_nop 1
	v_addc_co_u32_e32 v254, vcc, 0, v254, vcc
	v_cmp_ge_i32_e32 vcc, v250, v39
	s_nop 1
	v_addc_co_u32_e32 v254, vcc, 0, v254, vcc
	v_cmp_ge_i32_e32 vcc, v250, v40
	s_nop 1
	v_addc_co_u32_e32 v254, vcc, 0, v254, vcc
	v_cmp_ge_i32_e32 vcc, v250, v41
	s_nop 1
	v_addc_co_u32_e32 v254, vcc, 0, v254, vcc
	v_cmp_ge_i32_e32 vcc, v250, v42
	s_nop 1
	v_addc_co_u32_e32 v254, vcc, 0, v254, vcc
	v_cmp_ge_i32_e32 vcc, v250, v43
	s_nop 1
	v_addc_co_u32_e32 v254, vcc, 0, v254, vcc
	v_cmp_ge_i32_e32 vcc, v250, v44
	s_nop 1
	v_addc_co_u32_e32 v254, vcc, 0, v254, vcc
	v_cmp_ge_i32_e32 vcc, v250, v45
	s_nop 1
	v_addc_co_u32_e32 v254, vcc, 0, v254, vcc
	v_cmp_ge_i32_e32 vcc, v250, v46
	s_nop 1
	v_addc_co_u32_e32 v254, vcc, 0, v254, vcc
	v_cmp_ge_i32_e32 vcc, v250, v47
	s_nop 1
	v_addc_co_u32_e32 v254, vcc, 0, v254, vcc
	v_cmp_ge_i32_e32 vcc, v250, v48
	s_nop 1
	v_addc_co_u32_e32 v254, vcc, 0, v254, vcc
	v_cmp_ge_i32_e32 vcc, v250, v49
	s_nop 1
	v_addc_co_u32_e32 v254, vcc, 0, v254, vcc
	v_cmp_ge_i32_e32 vcc, v250, v50
	s_nop 1
	v_addc_co_u32_e32 v254, vcc, 0, v254, vcc
	v_cmp_ge_i32_e32 vcc, v250, v51
	s_nop 1
	v_addc_co_u32_e32 v254, vcc, 0, v254, vcc
	v_cmp_ge_i32_e32 vcc, v250, v52
	s_nop 1
	v_addc_co_u32_e32 v254, vcc, 0, v254, vcc
	v_cmp_ge_i32_e32 vcc, v250, v53
	s_nop 1
	v_addc_co_u32_e32 v254, vcc, 0, v254, vcc
	v_cmp_ge_i32_e32 vcc, v250, v54
	s_nop 1
	v_addc_co_u32_e32 v254, vcc, 0, v254, vcc
	v_cmp_ge_i32_e32 vcc, v250, v55
	s_nop 1
	v_addc_co_u32_e32 v254, vcc, 0, v254, vcc
	v_cmp_ge_i32_e32 vcc, v250, v56
	s_nop 1
	v_addc_co_u32_e32 v254, vcc, 0, v254, vcc
	v_cmp_ge_i32_e32 vcc, v250, v57
	s_nop 1
	v_addc_co_u32_e32 v254, vcc, 0, v254, vcc
	v_cmp_ge_i32_e32 vcc, v250, v58
	s_nop 1
	v_addc_co_u32_e32 v254, vcc, 0, v254, vcc
	v_cmp_ge_i32_e32 vcc, v250, v59
	s_nop 1
	v_addc_co_u32_e32 v254, vcc, 0, v254, vcc
	v_cmp_ge_i32_e32 vcc, v250, v60
	s_nop 1
	v_addc_co_u32_e32 v254, vcc, 0, v254, vcc
	v_cmp_ge_i32_e32 vcc, v250, v61
	s_nop 1
	v_addc_co_u32_e32 v254, vcc, 0, v254, vcc
	v_cmp_ge_i32_e32 vcc, v250, v62
	s_nop 1
	v_addc_co_u32_e32 v254, vcc, 0, v254, vcc
	v_cmp_ge_i32_e32 vcc, v250, v63
	s_nop 1
	v_addc_co_u32_e32 v254, vcc, 0, v254, vcc
	v_cmp_ge_i32_e32 vcc, v250, v64
	s_nop 1
	v_addc_co_u32_e32 v254, vcc, 0, v254, vcc
	s_barrier
	s_branch .LBB0_1435

.LBB0_1435:
	v_mov_b32_e32 v2, s99
	s_add_i32 s62, s62, 1
	s_mul_i32 s6, s62, s59
	s_add_i32 s11, s98, s6
	s_waitcnt lgkmcnt(0)
	v_cmp_ge_i32_e64 s[8:9], s11, v2
	v_cmp_lt_i32_e64 s[6:7], s11, v2
	s_and_b64 vcc, exec, s[8:9]
	s_cbranch_vccnz .LBB0_1446
	s_sub_i32 s11, s99, s11
	s_add_i32 s11, s11, -1
	s_mov_b32 s36, s11
	v_readlane_b32 s34, v254, s62
	s_mov_b64 s[38:39], -1
	s_and_b64 vcc, exec, s[8:9]
	s_cbranch_vccnz .LBB0_1447
